# S9: S4 + K3 log-softmax reductions via DPP row_ror instead of 8 dependent ds_bpermute round trips
# speedup vs baseline: 1.0092x; 1.0092x over previous
.Lk3_l1skipC:
	s_waitcnt vmcnt(18)
	v_cvt_f16_f32_e32 v104, v18
	s_waitcnt vmcnt(16)
	v_add_f32_e32 v18, v71, v72
	s_waitcnt vmcnt(15)
	v_fmac_f32_e32 v18, v54, v73
	v_div_scale_f32 v64, s[0:1], v18, v18, 1.0
	v_rcp_f32_e32 v65, v64
	s_waitcnt vmcnt(14)
	v_cvt_f16_f32_e32 v105, v33
	s_add_i32 s1, s15, 0x1200
	s_add_i32 s0, s15, 0x900
	v_fma_f32 v33, -v64, v65, 1.0
	v_fmac_f32_e32 v65, v33, v65
	v_div_scale_f32 v33, vcc, 1.0, v18, 1.0
	v_mul_f32_e32 v66, v33, v65
	v_fma_f32 v67, -v64, v66, v33
	v_fmac_f32_e32 v66, v67, v65
	v_fma_f32 v33, -v64, v66, v33
	v_div_fmas_f32 v33, v33, v65, v66
	s_waitcnt vmcnt(11)
	v_cvt_f32_f16_e32 v64, v34
	v_cvt_f32_f16_sdwa v65, v34 dst_sel:DWORD dst_unused:UNUSED_PAD src0_sel:WORD_1
	s_waitcnt vmcnt(10)
	v_cvt_f32_f16_e32 v66, v56
	v_cvt_f32_f16_sdwa v67, v56 dst_sel:DWORD dst_unused:UNUSED_PAD src0_sel:WORD_1
	s_waitcnt vmcnt(9)
	v_cvt_f32_f16_e32 v68, v60
	v_cvt_f32_f16_sdwa v69, v60 dst_sel:DWORD dst_unused:UNUSED_PAD src0_sel:WORD_1
	v_div_fixup_f32 v33, v33, v18, 1.0
	v_cmp_lt_f32_e32 vcc, 0, v18
	v_pk_add_f32 v[64:65], v[64:65], v[66:67]
	v_mul_u32_u24_e32 v34, 0x110, v70
	v_cndmask_b32_e32 v18, 0, v33, vcc
	v_pk_fma_f32 v[64:65], v[54:55], v[68:69], v[64:65] op_sel_hi:[0,1,1]
	v_pk_mul_f32 v[64:65], v[18:19], v[64:65] op_sel_hi:[0,1]
	v_mul_f32_e32 v33, 0x3fb8aa3b, v64
	v_exp_f32_e32 v66, v33
	v_mul_f32_e32 v33, 0x3fb8aa3b, v65
	v_exp_f32_e32 v67, v33
	v_mul_u32_u24_e32 v33, 0x440, v1
	v_add3_u32 v33, v33, v34, v98
	v_cvt_f32_f16_e32 v34, v35
	v_cvt_f32_f16_sdwa v35, v35 dst_sel:DWORD dst_unused:UNUSED_PAD src0_sel:WORD_1
	v_cvt_f32_f16_e32 v56, v57
	v_cvt_f32_f16_sdwa v57, v57 dst_sel:DWORD dst_unused:UNUSED_PAD src0_sel:WORD_1
	v_cvt_f32_f16_e32 v60, v61
	v_cvt_f32_f16_sdwa v61, v61 dst_sel:DWORD dst_unused:UNUSED_PAD src0_sel:WORD_1
	v_pk_add_f32 v[66:67], v[66:67], -1.0 op_sel_hi:[1,0]
	v_pk_add_f32 v[34:35], v[34:35], v[56:57]
	v_cmp_lt_f32_e32 vcc, 0, v65
	v_pk_fma_f32 v[34:35], v[54:55], v[60:61], v[34:35] op_sel_hi:[0,1,1]
	v_pk_mul_f32 v[56:57], v[18:19], v[34:35] op_sel_hi:[0,1]
	v_mul_f32_e32 v34, 0x3fb8aa3b, v56
	v_cndmask_b32_e32 v65, v67, v65, vcc
	v_exp_f32_e32 v60, v34
	v_mul_f32_e32 v34, 0x3fb8aa3b, v57
	v_cmp_lt_f32_e32 vcc, 0, v64
	v_exp_f32_e32 v61, v34
	v_cvt_f32_f16_sdwa v67, v58 dst_sel:DWORD dst_unused:UNUSED_PAD src0_sel:WORD_1
	v_cndmask_b32_e32 v34, v66, v64, vcc
	v_cvt_pk_f16_f32 v34, v34, v65
	v_cvt_f32_f16_e32 v64, v36
	v_cvt_f32_f16_sdwa v65, v36 dst_sel:DWORD dst_unused:UNUSED_PAD src0_sel:WORD_1
	v_cvt_f32_f16_e32 v66, v58
	v_cvt_f32_f16_e32 v68, v62
	v_cvt_f32_f16_sdwa v69, v62 dst_sel:DWORD dst_unused:UNUSED_PAD src0_sel:WORD_1
	v_pk_add_f32 v[60:61], v[60:61], -1.0 op_sel_hi:[1,0]
	v_pk_add_f32 v[64:65], v[64:65], v[66:67]
	v_cmp_lt_f32_e32 vcc, 0, v57
	v_pk_fma_f32 v[64:65], v[54:55], v[68:69], v[64:65] op_sel_hi:[0,1,1]
	v_pk_mul_f32 v[64:65], v[18:19], v[64:65] op_sel_hi:[0,1]
	v_mul_f32_e32 v36, 0x3fb8aa3b, v64
	v_cndmask_b32_e32 v35, v61, v57, vcc
	v_exp_f32_e32 v66, v36
	v_mul_f32_e32 v36, 0x3fb8aa3b, v65
	v_cmp_lt_f32_e32 vcc, 0, v56
	v_exp_f32_e32 v67, v36
	v_cvt_f32_f16_e32 v58, v59
	v_cndmask_b32_e32 v36, v60, v56, vcc
	v_cvt_pk_f16_f32 v35, v36, v35
	v_cvt_f32_f16_e32 v36, v37
	v_cvt_f32_f16_sdwa v37, v37 dst_sel:DWORD dst_unused:UNUSED_PAD src0_sel:WORD_1
	v_cvt_f32_f16_sdwa v59, v59 dst_sel:DWORD dst_unused:UNUSED_PAD src0_sel:WORD_1
	v_cvt_f32_f16_e32 v60, v63
	v_cvt_f32_f16_sdwa v61, v63 dst_sel:DWORD dst_unused:UNUSED_PAD src0_sel:WORD_1
	v_pk_add_f32 v[56:57], v[66:67], -1.0 op_sel_hi:[1,0]
	v_pk_add_f32 v[36:37], v[36:37], v[58:59]
	v_cmp_lt_f32_e32 vcc, 0, v65
	v_pk_fma_f32 v[36:37], v[54:55], v[60:61], v[36:37] op_sel_hi:[0,1,1]
	v_pk_mul_f32 v[58:59], v[18:19], v[36:37] op_sel_hi:[0,1]
	v_mul_f32_e32 v36, 0x3fb8aa3b, v58
	v_cndmask_b32_e32 v57, v57, v65, vcc
	v_exp_f32_e32 v60, v36
	v_mul_f32_e32 v36, 0x3fb8aa3b, v59
	v_cmp_lt_f32_e32 vcc, 0, v64
	v_exp_f32_e32 v61, v36
	s_waitcnt vmcnt(1)
	v_cvt_f32_f16_e32 v62, v42
	v_cndmask_b32_e32 v36, v56, v64, vcc
	v_cvt_pk_f16_f32 v36, v36, v57
	v_cvt_f32_f16_e32 v56, v46
	v_cvt_f32_f16_sdwa v57, v46 dst_sel:DWORD dst_unused:UNUSED_PAD src0_sel:WORD_1
	v_cvt_f32_f16_sdwa v63, v42 dst_sel:DWORD dst_unused:UNUSED_PAD src0_sel:WORD_1
	s_mul_hi_i32 s1, s1, 0x4bda12f7
	s_waitcnt vmcnt(0)
	v_cvt_f32_f16_e32 v64, v38
	v_cvt_f32_f16_sdwa v65, v38 dst_sel:DWORD dst_unused:UNUSED_PAD src0_sel:WORD_1
	s_lshr_b32 s6, s1, 31
	s_ashr_i32 s1, s1, 3
	s_mul_hi_i32 s0, s0, 0x4bda12f7
	s_add_i32 s10, s1, s6
	s_lshr_b32 s1, s0, 31
	s_ashr_i32 s0, s0, 3
	s_add_i32 s6, s0, s1
	v_pk_add_f32 v[56:57], v[56:57], v[62:63]
	s_mul_i32 s11, s6, 27
	v_pk_fma_f32 v[56:57], v[54:55], v[64:65], v[56:57] op_sel_hi:[0,1,1]
	s_mul_hi_i32 s0, s11, 0x2aaaaaab
	v_pk_mul_f32 v[56:57], v[18:19], v[56:57] op_sel_hi:[0,1]
	s_lshr_b32 s1, s0, 31
	s_ashr_i32 s0, s0, 3
	v_pk_add_f32 v[60:61], v[60:61], -1.0 op_sel_hi:[1,0]
	v_cmp_lt_f32_e32 vcc, 0, v59
	v_mul_f32_e32 v38, 0x3fb8aa3b, v56
	s_lshl_b32 s7, s6, 1
	s_add_i32 s0, s0, s1
	v_cndmask_b32_e32 v37, v61, v59, vcc
	v_exp_f32_e32 v62, v38
	v_mul_f32_e32 v38, 0x3fb8aa3b, v57
	v_cmp_lt_f32_e32 vcc, 0, v58
	s_cmp_lg_u32 s0, s16
	v_exp_f32_e32 v63, v38
	v_cndmask_b32_e32 v38, v60, v58, vcc
	s_cselect_b64 s[0:1], -1, 0
	s_add_i32 s11, s11, 27
	v_cvt_pk_f16_f32 v37, v38, v37
	v_cndmask_b32_e64 v38, 0, 1, s[0:1]
	s_mul_hi_i32 s0, s11, 0x2aaaaaab
	v_or_b32_e32 v60, s7, v38
	s_lshr_b32 s1, s0, 31
	s_ashr_i32 s0, s0, 3
	v_ashrrev_i32_e32 v61, 31, v60
	s_add_i32 s0, s0, s1
	v_lshlrev_b64 v[60:61], 6, v[60:61]
	s_cmp_lg_u32 s0, s16
	v_or_b32_e32 v38, v60, v55
	s_cselect_b64 s[0:1], -1, 0
	v_or_b32_e32 v60, s14, v38
	v_cndmask_b32_e64 v38, 0, 1, s[0:1]
	s_add_i32 s0, s15, 0x92f
	s_addk_i32 s15, 0x122f
	s_mul_hi_i32 s1, s15, 0x4bda12f7
	v_or_b32_e32 v38, s7, v38
	s_lshr_b32 s7, s1, 31
	s_ashr_i32 s1, s1, 3
	s_mul_hi_i32 s0, s0, 0x4bda12f7
	s_add_i32 s13, s1, s7
	s_lshr_b32 s1, s0, 31
	s_ashr_i32 s0, s0, 3
	s_add_i32 s7, s0, s1
	s_mul_i32 s0, s7, 27
	s_mul_hi_i32 s0, s0, 0x2aaaaaab
	v_pk_add_f32 v[58:59], v[62:63], -1.0 op_sel_hi:[1,0]
	v_add_u32_e32 v62, 2, v38
	s_lshr_b32 s1, s0, 31
	s_ashr_i32 s0, s0, 3
	v_ashrrev_i32_e32 v63, 31, v62
	s_lshl_b32 s11, s7, 1
	s_add_i32 s0, s0, s1
	v_lshlrev_b64 v[62:63], 6, v[62:63]
	s_cmp_lg_u32 s0, s16
	v_or_b32_e32 v38, v62, v55
	s_cselect_b64 s[0:1], -1, 0
	v_or_b32_e32 v62, s14, v38
	v_cndmask_b32_e64 v38, 0, 1, s[0:1]
	s_sub_i32 s6, s7, s6
	s_sub_i32 s0, s13, s10
	s_cmp_eq_u32 s0, 2
	s_cselect_b64 s[0:1], -1, 0
	s_cmp_eq_u32 s6, 2
	s_mul_i32 s16, s10, 27
	s_cselect_b64 s[6:7], -1, 0
	s_lshl_b32 s15, s10, 1
	s_mul_hi_i32 s10, s16, 0x2aaaaaab
	v_or_b32_e32 v64, s11, v38
	s_lshr_b32 s11, s10, 31
	s_ashr_i32 s10, s10, 3
	v_ashrrev_i32_e32 v65, 31, v64
	s_add_i32 s10, s10, s11
	v_lshlrev_b64 v[64:65], 6, v[64:65]
	s_cmp_lg_u32 s10, s12
	v_or_b32_e32 v38, v64, v55
	s_cselect_b64 s[10:11], -1, 0
	s_add_i32 s16, s16, 27
	v_or_b32_e32 v64, s14, v38
	v_lshl_add_u64 v[66:67], v[60:61], 4, v[52:53]
	v_cndmask_b32_e64 v38, 0, 1, s[10:11]
	s_mul_hi_i32 s10, s16, 0x2aaaaaab
	v_lshl_add_u64 v[68:69], v[62:63], 4, v[52:53]
	v_lshl_add_u64 v[70:71], v[64:65], 4, v[52:53]
	global_load_dword v73, v[66:67], off
	global_load_dword v83, v[68:69], off
	global_load_dword v97, v[70:71], off
	v_or_b32_e32 v66, s15, v38
	s_lshr_b32 s11, s10, 31
	s_ashr_i32 s10, s10, 3
	v_ashrrev_i32_e32 v67, 31, v66
	s_add_i32 s10, s10, s11
	v_lshlrev_b64 v[70:71], 6, v[66:67]
	s_cmp_lg_u32 s10, s12
	v_or_b32_e32 v38, v70, v55
	s_cselect_b64 s[10:11], -1, 0
	v_or_b32_e32 v70, s14, v38
	v_cndmask_b32_e64 v38, 0, 1, s[10:11]
	v_or_b32_e32 v38, s15, v38
	s_lshl_b32 s15, s13, 1
	s_mul_i32 s13, s13, 27
	s_mul_hi_i32 s10, s13, 0x2aaaaaab
	v_add_u32_e32 v66, 2, v38
	s_lshr_b32 s11, s10, 31
	s_ashr_i32 s10, s10, 3
	v_ashrrev_i32_e32 v67, 31, v66
	s_add_i32 s10, s10, s11
	v_lshlrev_b64 v[102:103], 6, v[66:67]
	s_cmp_lg_u32 s10, s12
	v_or_b32_e32 v38, v102, v55
	s_cselect_b64 s[10:11], -1, 0
	v_or_b32_e32 v102, s14, v38
	v_cndmask_b32_e64 v38, 0, 1, s[10:11]
	v_or_b32_e32 v66, s15, v38
	v_ashrrev_i32_e32 v67, 31, v66
	v_lshlrev_b64 v[108:109], 6, v[66:67]
	v_or_b32_e32 v38, v108, v55
	v_or_b32_e32 v108, s14, v38
	v_lshl_add_u64 v[66:67], v[70:71], 4, v[52:53]
	v_lshl_add_u64 v[68:69], v[102:103], 4, v[52:53]
	v_lshl_add_u64 v[52:53], v[108:109], 4, v[52:53]
	global_load_dword v72, v[66:67], off
	global_load_dword v82, v[68:69], off
	global_load_dword v96, v[52:53], off
	v_cvt_f32_f16_e32 v46, v47
	v_cvt_f32_f16_sdwa v47, v47 dst_sel:DWORD dst_unused:UNUSED_PAD src0_sel:WORD_1
	v_cvt_f32_f16_e32 v42, v43
	v_cvt_f32_f16_sdwa v43, v43 dst_sel:DWORD dst_unused:UNUSED_PAD src0_sel:WORD_1
	v_cvt_f32_f16_e32 v38, v39
	v_cvt_f32_f16_sdwa v39, v39 dst_sel:DWORD dst_unused:UNUSED_PAD src0_sel:WORD_1
	v_cmp_lt_f32_e32 vcc, 0, v57
	v_pk_add_f32 v[42:43], v[46:47], v[42:43]
	v_cvt_f16_f32_e32 v26, v26
	v_cndmask_b32_e32 v55, v59, v57, vcc
	v_pk_fma_f32 v[38:39], v[54:55], v[38:39], v[42:43] op_sel_hi:[0,1,1]
	v_pk_mul_f32 v[42:43], v[18:19], v[38:39] op_sel_hi:[0,1]
	v_mul_f32_e32 v38, 0x3fb8aa3b, v42
	v_exp_f32_e32 v46, v38
	v_mul_f32_e32 v38, 0x3fb8aa3b, v43
	v_exp_f32_e32 v47, v38
	v_lshlrev_b64 v[38:39], 9, v[60:61]
	v_lshl_add_u64 v[52:53], v[50:51], 0, v[38:39]
	v_lshlrev_b64 v[38:39], 9, v[62:63]
	v_lshl_add_u64 v[60:61], v[50:51], 0, v[38:39]
	v_lshlrev_b64 v[38:39], 9, v[64:65]
	global_load_dwordx4 v[84:87], v[52:53], off
	v_lshl_add_u64 v[62:63], v[50:51], 0, v[38:39]
	global_load_dwordx4 v[88:91], v[60:61], off
	global_load_dwordx4 v[92:95], v[62:63], off
	global_load_dwordx4 v[78:81], v[52:53], off offset:64
	global_load_dwordx4 v[74:77], v[60:61], off offset:64
	global_load_dwordx4 v[66:69], v[62:63], off offset:64
	v_cmp_lt_f32_e32 vcc, 0, v56
	v_cvt_f32_f16_sdwa v57, v48 dst_sel:DWORD dst_unused:UNUSED_PAD src0_sel:WORD_1
	v_cvt_f32_f16_sdwa v59, v44 dst_sel:DWORD dst_unused:UNUSED_PAD src0_sel:WORD_1
	v_cndmask_b32_e32 v38, v58, v56, vcc
	v_cvt_f32_f16_e32 v56, v48
	v_cvt_f32_f16_e32 v58, v44
	v_cvt_f32_f16_e32 v64, v40
	v_cvt_f32_f16_sdwa v65, v40 dst_sel:DWORD dst_unused:UNUSED_PAD src0_sel:WORD_1
	v_pk_add_f32 v[46:47], v[46:47], -1.0 op_sel_hi:[1,0]
	v_pk_add_f32 v[56:57], v[56:57], v[58:59]
	v_cmp_lt_f32_e32 vcc, 0, v43
	v_pk_fma_f32 v[56:57], v[54:55], v[64:65], v[56:57] op_sel_hi:[0,1,1]
	v_pk_mul_f32 v[56:57], v[18:19], v[56:57] op_sel_hi:[0,1]
	v_mul_f32_e32 v40, 0x3fb8aa3b, v56
	v_cndmask_b32_e32 v39, v47, v43, vcc
	v_exp_f32_e32 v58, v40
	v_mul_f32_e32 v40, 0x3fb8aa3b, v57
	v_cmp_lt_f32_e32 vcc, 0, v42
	v_exp_f32_e32 v59, v40
	v_cvt_f32_f16_sdwa v47, v49 dst_sel:DWORD dst_unused:UNUSED_PAD src0_sel:WORD_1
	v_cndmask_b32_e32 v40, v46, v42, vcc
	v_cvt_f32_f16_e32 v46, v49
	v_cvt_f32_f16_e32 v44, v45
	v_cvt_f32_f16_sdwa v45, v45 dst_sel:DWORD dst_unused:UNUSED_PAD src0_sel:WORD_1
	v_cvt_pk_f16_f32 v39, v40, v39
	v_cvt_f32_f16_e32 v40, v41
	v_cvt_f32_f16_sdwa v41, v41 dst_sel:DWORD dst_unused:UNUSED_PAD src0_sel:WORD_1
	v_pk_add_f32 v[44:45], v[46:47], v[44:45]
	v_pk_add_f32 v[42:43], v[58:59], -1.0 op_sel_hi:[1,0]
	v_cmp_lt_f32_e32 vcc, 0, v57
	v_pk_fma_f32 v[40:41], v[54:55], v[40:41], v[44:45] op_sel_hi:[0,1,1]
	v_pk_mul_f32 v[44:45], v[18:19], v[40:41] op_sel_hi:[0,1]
	v_mul_f32_e32 v18, 0x3fb8aa3b, v44
	v_exp_f32_e32 v46, v18
	v_mul_f32_e32 v18, 0x3fb8aa3b, v45
	v_exp_f32_e32 v47, v18
	v_cndmask_b32_e32 v43, v43, v57, vcc
	v_cmp_lt_f32_e32 vcc, 0, v56
	v_cvt_pk_f16_f32 v38, v38, v55
	v_cvt_f16_f32_e32 v25, v25
	v_cndmask_b32_e32 v18, v42, v56, vcc
	v_cvt_pk_f16_f32 v40, v18, v43
	v_pk_add_f32 v[42:43], v[46:47], -1.0 op_sel_hi:[1,0]
	v_cmp_lt_f32_e32 vcc, 0, v45
	s_waitcnt vmcnt(3)
	v_cvt_f32_f16_sdwa v53, v92 dst_sel:DWORD dst_unused:UNUSED_PAD src0_sel:WORD_1
	v_cndmask_b32_e32 v18, v43, v45, vcc
	v_cmp_lt_f32_e32 vcc, 0, v44
	s_nop 1
	v_cndmask_b32_e32 v41, v42, v44, vcc
	v_lshlrev_b64 v[42:43], 9, v[70:71]
	v_lshl_add_u64 v[46:47], v[50:51], 0, v[42:43]
	v_lshlrev_b64 v[42:43], 9, v[102:103]
	v_cndmask_b32_e64 v103, 0, 1.0, s[6:7]
	v_cndmask_b32_e64 v102, 0, 1.0, s[0:1]
	v_pk_add_f32 v[44:45], v[72:73], v[82:83]
	v_cvt_pk_f16_f32 v41, v41, v18
	v_pk_fma_f32 v[82:83], v[102:103], v[96:97], v[44:45]
	v_lshl_add_u64 v[48:49], v[50:51], 0, v[42:43]
	v_div_scale_f32 v18, s[0:1], v83, v83, 1.0
	v_rcp_f32_e32 v52, v18
	v_lshlrev_b64 v[42:43], 9, v[108:109]
	v_lshl_add_u64 v[96:97], v[50:51], 0, v[42:43]
	global_load_dwordx4 v[58:61], v[46:47], off
	global_load_dwordx4 v[42:45], v[46:47], off offset:64
	v_fma_f32 v46, -v18, v52, 1.0
	v_fmac_f32_e32 v52, v46, v52
	v_div_scale_f32 v46, vcc, 1.0, v83, 1.0
	v_mul_f32_e32 v47, v46, v52
	v_fma_f32 v50, -v18, v47, v46
	v_fmac_f32_e32 v47, v50, v52
	v_fma_f32 v18, -v18, v47, v46
	v_div_fmas_f32 v18, v18, v52, v47
	v_cvt_f32_f16_e32 v46, v84
	v_cvt_f32_f16_sdwa v47, v84 dst_sel:DWORD dst_unused:UNUSED_PAD src0_sel:WORD_1
	v_cvt_f32_f16_e32 v50, v88
	v_cvt_f32_f16_sdwa v51, v88 dst_sel:DWORD dst_unused:UNUSED_PAD src0_sel:WORD_1
	v_cvt_f32_f16_e32 v52, v92
	v_div_fixup_f32 v18, v18, v83, 1.0
	v_cmp_lt_f32_e32 vcc, 0, v83
	v_pk_add_f32 v[46:47], v[46:47], v[50:51]
	v_mov_b32_e32 v84, v103
	v_cndmask_b32_e32 v18, 0, v18, vcc
	v_pk_fma_f32 v[46:47], v[84:85], v[52:53], v[46:47] op_sel_hi:[0,1,1]
	v_pk_mul_f32 v[46:47], v[18:19], v[46:47] op_sel_hi:[0,1]
	v_mul_f32_e32 v50, 0x3fb8aa3b, v46
	v_exp_f32_e32 v108, v50
	v_mul_f32_e32 v50, 0x3fb8aa3b, v47
	v_exp_f32_e32 v109, v50
	global_load_dwordx4 v[70:73], v[48:49], off
	global_load_dwordx4 v[50:53], v[48:49], off offset:64
	global_load_dwordx4 v[62:65], v[96:97], off
	global_load_dwordx4 v[54:57], v[96:97], off offset:64
	v_cvt_f32_f16_e32 v96, v85
	v_cvt_f32_f16_sdwa v97, v85 dst_sel:DWORD dst_unused:UNUSED_PAD src0_sel:WORD_1
	v_cvt_f32_f16_e32 v88, v89
	v_cvt_f32_f16_sdwa v89, v89 dst_sel:DWORD dst_unused:UNUSED_PAD src0_sel:WORD_1
	v_cvt_f32_f16_e32 v92, v93
	v_cvt_f32_f16_sdwa v93, v93 dst_sel:DWORD dst_unused:UNUSED_PAD src0_sel:WORD_1
	v_pk_add_f32 v[48:49], v[108:109], -1.0 op_sel_hi:[1,0]
	v_pk_add_f32 v[88:89], v[96:97], v[88:89]
	v_cmp_lt_f32_e32 vcc, 0, v47
	v_pk_fma_f32 v[88:89], v[84:85], v[92:93], v[88:89] op_sel_hi:[0,1,1]
	v_pk_mul_f32 v[88:89], v[18:19], v[88:89] op_sel_hi:[0,1]
	v_cndmask_b32_e32 v47, v49, v47, vcc
	v_mul_f32_e32 v49, 0x3fb8aa3b, v88
	v_exp_f32_e32 v92, v49
	v_mul_f32_e32 v49, 0x3fb8aa3b, v89
	v_exp_f32_e32 v93, v49
	v_cmp_lt_f32_e32 vcc, 0, v46
	v_cvt_f32_f16_e32 v96, v90
	v_cvt_f32_f16_sdwa v97, v90 dst_sel:DWORD dst_unused:UNUSED_PAD src0_sel:WORD_1
	v_cndmask_b32_e32 v46, v48, v46, vcc
	v_pk_add_f32 v[48:49], v[92:93], -1.0 op_sel_hi:[1,0]
	v_cvt_f32_f16_e32 v92, v86
	v_cvt_f32_f16_sdwa v93, v86 dst_sel:DWORD dst_unused:UNUSED_PAD src0_sel:WORD_1
	v_cvt_f32_f16_e32 v108, v94
	v_cvt_f32_f16_sdwa v109, v94 dst_sel:DWORD dst_unused:UNUSED_PAD src0_sel:WORD_1
	v_cmp_lt_f32_e32 vcc, 0, v89
	v_pk_add_f32 v[92:93], v[92:93], v[96:97]
	v_cvt_pk_f16_f32 v46, v46, v47
	v_pk_fma_f32 v[92:93], v[84:85], v[108:109], v[92:93] op_sel_hi:[0,1,1]
	v_pk_mul_f32 v[92:93], v[18:19], v[92:93] op_sel_hi:[0,1]
	v_cndmask_b32_e32 v47, v49, v89, vcc
	v_mul_f32_e32 v49, 0x3fb8aa3b, v92
	v_exp_f32_e32 v96, v49
	v_mul_f32_e32 v49, 0x3fb8aa3b, v93
	v_cmp_lt_f32_e32 vcc, 0, v88
	v_exp_f32_e32 v97, v49
	v_cvt_f32_f16_e32 v86, v87
	v_cndmask_b32_e32 v48, v48, v88, vcc
	v_cvt_f32_f16_sdwa v87, v87 dst_sel:DWORD dst_unused:UNUSED_PAD src0_sel:WORD_1
	v_cvt_f32_f16_e32 v88, v91
	v_cvt_f32_f16_sdwa v89, v91 dst_sel:DWORD dst_unused:UNUSED_PAD src0_sel:WORD_1
	v_cvt_f32_f16_e32 v90, v95
	v_cvt_f32_f16_sdwa v91, v95 dst_sel:DWORD dst_unused:UNUSED_PAD src0_sel:WORD_1
	v_cvt_pk_f16_f32 v47, v48, v47
	v_pk_add_f32 v[48:49], v[96:97], -1.0 op_sel_hi:[1,0]
	v_cmp_lt_f32_e32 vcc, 0, v93
	v_pk_add_f32 v[86:87], v[86:87], v[88:89]
	s_waitcnt vmcnt(6)
	v_cvt_f32_f16_e32 v94, v66
	v_cndmask_b32_e32 v49, v49, v93, vcc
	v_pk_fma_f32 v[86:87], v[84:85], v[90:91], v[86:87] op_sel_hi:[0,1,1]
	v_cmp_lt_f32_e32 vcc, 0, v92
	v_pk_mul_f32 v[86:87], v[18:19], v[86:87] op_sel_hi:[0,1]
	v_cvt_f32_f16_e32 v90, v78
	v_cndmask_b32_e32 v48, v48, v92, vcc
	v_cvt_f32_f16_sdwa v91, v78 dst_sel:DWORD dst_unused:UNUSED_PAD src0_sel:WORD_1
	v_cvt_f32_f16_e32 v92, v74
	v_cvt_f32_f16_sdwa v93, v74 dst_sel:DWORD dst_unused:UNUSED_PAD src0_sel:WORD_1
	v_mul_f32_e32 v83, 0x3fb8aa3b, v86
	v_cvt_f32_f16_sdwa v95, v66 dst_sel:DWORD dst_unused:UNUSED_PAD src0_sel:WORD_1
	v_exp_f32_e32 v88, v83
	v_mul_f32_e32 v83, 0x3fb8aa3b, v87
	v_exp_f32_e32 v89, v83
	v_pk_add_f32 v[90:91], v[90:91], v[92:93]
	v_cmp_lt_f32_e32 vcc, 0, v87
	v_pk_fma_f32 v[90:91], v[84:85], v[94:95], v[90:91] op_sel_hi:[0,1,1]
	v_pk_mul_f32 v[90:91], v[18:19], v[90:91] op_sel_hi:[0,1]
	v_pk_add_f32 v[88:89], v[88:89], -1.0 op_sel_hi:[1,0]
	v_mul_f32_e32 v66, 0x3fb8aa3b, v90
	v_cvt_pk_f16_f32 v48, v48, v49
	v_cndmask_b32_e32 v49, v89, v87, vcc
	v_exp_f32_e32 v92, v66
	v_mul_f32_e32 v66, 0x3fb8aa3b, v91
	v_cmp_lt_f32_e32 vcc, 0, v86
	v_exp_f32_e32 v93, v66
	v_cvt_f32_f16_e32 v78, v79
	v_cndmask_b32_e32 v66, v88, v86, vcc
	v_cvt_f32_f16_sdwa v79, v79 dst_sel:DWORD dst_unused:UNUSED_PAD src0_sel:WORD_1
	v_cvt_f32_f16_e32 v74, v75
	v_cvt_f32_f16_sdwa v75, v75 dst_sel:DWORD dst_unused:UNUSED_PAD src0_sel:WORD_1
	v_cvt_pk_f16_f32 v49, v66, v49
	v_cvt_f32_f16_e32 v66, v67
	v_cvt_f32_f16_sdwa v67, v67 dst_sel:DWORD dst_unused:UNUSED_PAD src0_sel:WORD_1
	v_pk_add_f32 v[74:75], v[78:79], v[74:75]
	v_pk_add_f32 v[86:87], v[92:93], -1.0 op_sel_hi:[1,0]
	v_cmp_lt_f32_e32 vcc, 0, v91
	v_pk_fma_f32 v[66:67], v[84:85], v[66:67], v[74:75] op_sel_hi:[0,1,1]
	v_pk_mul_f32 v[74:75], v[18:19], v[66:67] op_sel_hi:[0,1]
	v_mul_f32_e32 v66, 0x3fb8aa3b, v74
	v_cndmask_b32_e32 v83, v87, v91, vcc
	v_exp_f32_e32 v78, v66
	v_mul_f32_e32 v66, 0x3fb8aa3b, v75
	v_cmp_lt_f32_e32 vcc, 0, v90
	v_exp_f32_e32 v79, v66
	v_cvt_f32_f16_sdwa v87, v80 dst_sel:DWORD dst_unused:UNUSED_PAD src0_sel:WORD_1
	v_cndmask_b32_e32 v66, v86, v90, vcc
	v_cvt_f32_f16_e32 v86, v80
	v_cvt_f32_f16_e32 v88, v76
	v_cvt_f32_f16_sdwa v89, v76 dst_sel:DWORD dst_unused:UNUSED_PAD src0_sel:WORD_1
	v_cvt_f32_f16_e32 v90, v68
	v_cvt_f32_f16_sdwa v91, v68 dst_sel:DWORD dst_unused:UNUSED_PAD src0_sel:WORD_1
	v_pk_add_f32 v[78:79], v[78:79], -1.0 op_sel_hi:[1,0]
	v_pk_add_f32 v[86:87], v[86:87], v[88:89]
	v_cmp_lt_f32_e32 vcc, 0, v75
	v_pk_fma_f32 v[86:87], v[84:85], v[90:91], v[86:87] op_sel_hi:[0,1,1]
	v_pk_mul_f32 v[86:87], v[18:19], v[86:87] op_sel_hi:[0,1]
	v_mul_f32_e32 v68, 0x3fb8aa3b, v86
	v_exp_f32_e32 v88, v68
	v_mul_f32_e32 v68, 0x3fb8aa3b, v87
	v_exp_f32_e32 v89, v68
	v_cndmask_b32_e32 v67, v79, v75, vcc
	v_cmp_lt_f32_e32 vcc, 0, v74
	v_cvt_f32_f16_sdwa v79, v81 dst_sel:DWORD dst_unused:UNUSED_PAD src0_sel:WORD_1
	v_cvt_f32_f16_e32 v76, v77
	v_cndmask_b32_e32 v68, v78, v74, vcc
	v_cvt_f32_f16_e32 v78, v81
	v_cvt_f32_f16_sdwa v77, v77 dst_sel:DWORD dst_unused:UNUSED_PAD src0_sel:WORD_1
	v_cvt_f32_f16_e32 v80, v69
	v_cvt_f32_f16_sdwa v81, v69 dst_sel:DWORD dst_unused:UNUSED_PAD src0_sel:WORD_1
	v_pk_add_f32 v[74:75], v[88:89], -1.0 op_sel_hi:[1,0]
	v_cmp_lt_f32_e32 vcc, 0, v87
	v_cvt_pk_f16_f32 v67, v68, v67
	v_cvt_pk_f16_f32 v66, v66, v83
	v_cndmask_b32_e32 v68, v75, v87, vcc
	v_cmp_lt_f32_e32 vcc, 0, v86
	s_waitcnt vmcnt(2)
	v_cvt_f32_f16_sdwa v107, v52 dst_sel:DWORD dst_unused:UNUSED_PAD src0_sel:WORD_1
	v_cndmask_b32_e32 v69, v74, v86, vcc
	v_pk_add_f32 v[74:75], v[78:79], v[76:77]
	v_cvt_pk_f16_f32 v68, v69, v68
	v_pk_fma_f32 v[74:75], v[84:85], v[80:81], v[74:75] op_sel_hi:[0,1,1]
	v_pk_mul_f32 v[74:75], v[18:19], v[74:75] op_sel_hi:[0,1]
	v_mul_f32_e32 v18, 0x3fb8aa3b, v74
	v_exp_f32_e32 v76, v18
	v_mul_f32_e32 v18, 0x3fb8aa3b, v75
	v_exp_f32_e32 v77, v18
	v_div_scale_f32 v18, s[0:1], v82, v82, 1.0
	v_rcp_f32_e32 v69, v18
	v_pk_add_f32 v[76:77], v[76:77], -1.0 op_sel_hi:[1,0]
	v_cmp_lt_f32_e32 vcc, 0, v75
	v_cvt_f32_f16_e32 v80, v70
	v_cvt_f32_f16_sdwa v81, v70 dst_sel:DWORD dst_unused:UNUSED_PAD src0_sel:WORD_1
	v_cndmask_b32_e32 v75, v77, v75, vcc
	v_fma_f32 v77, -v18, v69, 1.0
	v_fmac_f32_e32 v69, v77, v69
	v_div_scale_f32 v77, vcc, 1.0, v82, 1.0
	v_mul_f32_e32 v78, v77, v69
	v_fma_f32 v79, -v18, v78, v77
	v_fmac_f32_e32 v78, v79, v69
	v_fma_f32 v18, -v18, v78, v77
	v_div_fmas_f32 v18, v18, v69, v78
	v_cvt_f32_f16_e32 v78, v58
	v_cvt_f32_f16_sdwa v79, v58 dst_sel:DWORD dst_unused:UNUSED_PAD src0_sel:WORD_1
	s_waitcnt vmcnt(1)
	v_cvt_f32_f16_e32 v84, v62
	v_cvt_f32_f16_sdwa v85, v62 dst_sel:DWORD dst_unused:UNUSED_PAD src0_sel:WORD_1
	v_div_fixup_f32 v18, v18, v82, 1.0
	v_cmp_lt_f32_e32 vcc, 0, v82
	v_pk_add_f32 v[78:79], v[78:79], v[80:81]
	v_cvt_f32_f16_e32 v70, v71
	v_cndmask_b32_e32 v18, 0, v18, vcc
	v_pk_fma_f32 v[78:79], v[102:103], v[84:85], v[78:79] op_sel_hi:[0,1,1]
	v_pk_mul_f32 v[78:79], v[18:19], v[78:79] op_sel_hi:[0,1]
	v_mul_f32_e32 v58, 0x3fb8aa3b, v78
	v_exp_f32_e32 v80, v58
	v_mul_f32_e32 v58, 0x3fb8aa3b, v79
	v_exp_f32_e32 v81, v58
	v_cmp_lt_f32_e32 vcc, 0, v74
	v_cvt_f32_f16_sdwa v71, v71 dst_sel:DWORD dst_unused:UNUSED_PAD src0_sel:WORD_1
	v_cvt_f32_f16_e32 v62, v63
	v_cndmask_b32_e32 v58, v76, v74, vcc
	v_cvt_pk_f16_f32 v69, v58, v75
	v_cvt_f32_f16_e32 v58, v59
	v_cvt_f32_f16_sdwa v59, v59 dst_sel:DWORD dst_unused:UNUSED_PAD src0_sel:WORD_1
	v_cvt_f32_f16_sdwa v63, v63 dst_sel:DWORD dst_unused:UNUSED_PAD src0_sel:WORD_1
	v_pk_add_f32 v[74:75], v[80:81], -1.0 op_sel_hi:[1,0]
	v_cmp_lt_f32_e32 vcc, 0, v79
	v_pk_add_f32 v[58:59], v[58:59], v[70:71]
	v_cvt_f32_f16_sdwa v71, v60 dst_sel:DWORD dst_unused:UNUSED_PAD src0_sel:WORD_1
	v_cndmask_b32_e32 v75, v75, v79, vcc
	v_cmp_lt_f32_e32 vcc, 0, v78
	v_pk_fma_f32 v[58:59], v[102:103], v[62:63], v[58:59] op_sel_hi:[0,1,1]
	v_pk_mul_f32 v[58:59], v[18:19], v[58:59] op_sel_hi:[0,1]
	v_cndmask_b32_e32 v70, v74, v78, vcc
	v_cvt_pk_f16_f32 v94, v70, v75
	v_cvt_f32_f16_e32 v70, v60
	v_cvt_f32_f16_e32 v74, v72
	v_cvt_f32_f16_sdwa v75, v72 dst_sel:DWORD dst_unused:UNUSED_PAD src0_sel:WORD_1
	v_cvt_f32_f16_e32 v76, v64
	v_cvt_f32_f16_sdwa v77, v64 dst_sel:DWORD dst_unused:UNUSED_PAD src0_sel:WORD_1
	v_mul_f32_e32 v62, 0x3fb8aa3b, v58
	v_mul_f32_e32 v63, 0x3fb8aa3b, v59
	v_exp_f32_e32 v62, v62
	v_exp_f32_e32 v63, v63
	v_pk_add_f32 v[70:71], v[70:71], v[74:75]
	v_cmp_lt_f32_e32 vcc, 0, v59
	v_pk_fma_f32 v[70:71], v[102:103], v[76:77], v[70:71] op_sel_hi:[0,1,1]
	v_pk_mul_f32 v[70:71], v[18:19], v[70:71] op_sel_hi:[0,1]
	v_pk_add_f32 v[62:63], v[62:63], -1.0 op_sel_hi:[1,0]
	v_mul_f32_e32 v60, 0x3fb8aa3b, v70
	v_cndmask_b32_e32 v59, v63, v59, vcc
	v_exp_f32_e32 v74, v60
	v_mul_f32_e32 v60, 0x3fb8aa3b, v71
	v_cmp_lt_f32_e32 vcc, 0, v58
	v_exp_f32_e32 v75, v60
	v_cvt_f32_f16_e32 v60, v61
	v_cndmask_b32_e32 v58, v62, v58, vcc
	v_cvt_f32_f16_sdwa v61, v61 dst_sel:DWORD dst_unused:UNUSED_PAD src0_sel:WORD_1
	v_cvt_f32_f16_e32 v62, v73
	v_cvt_f32_f16_sdwa v63, v73 dst_sel:DWORD dst_unused:UNUSED_PAD src0_sel:WORD_1
	v_cvt_f32_f16_e32 v64, v65
	v_cvt_f32_f16_sdwa v65, v65 dst_sel:DWORD dst_unused:UNUSED_PAD src0_sel:WORD_1
	v_cvt_pk_f16_f32 v95, v58, v59
	v_pk_add_f32 v[60:61], v[60:61], v[62:63]
	v_pk_add_f32 v[58:59], v[74:75], -1.0 op_sel_hi:[1,0]
	v_pk_fma_f32 v[60:61], v[102:103], v[64:65], v[60:61] op_sel_hi:[0,1,1]
	v_pk_mul_f32 v[60:61], v[18:19], v[60:61] op_sel_hi:[0,1]
	v_mul_f32_e32 v62, 0x3fb8aa3b, v60
	v_mul_f32_e32 v63, 0x3fb8aa3b, v61
	v_exp_f32_e32 v62, v62
	v_exp_f32_e32 v63, v63
	v_cmp_lt_f32_e32 vcc, 0, v71
	v_cvt_f32_f16_e32 v64, v50
	v_cvt_f32_f16_sdwa v65, v50 dst_sel:DWORD dst_unused:UNUSED_PAD src0_sel:WORD_1
	v_cndmask_b32_e32 v59, v59, v71, vcc
	v_cmp_lt_f32_e32 vcc, 0, v70
	s_waitcnt vmcnt(0)
	v_cvt_f32_f16_sdwa v71, v54 dst_sel:DWORD dst_unused:UNUSED_PAD src0_sel:WORD_1
	s_movk_i32 s0, 0xc4
	v_cndmask_b32_e32 v58, v58, v70, vcc
	v_cvt_pk_f16_f32 v96, v58, v59
	v_pk_add_f32 v[58:59], v[62:63], -1.0 op_sel_hi:[1,0]
	v_cvt_f32_f16_e32 v62, v42
	v_cvt_f32_f16_sdwa v63, v42 dst_sel:DWORD dst_unused:UNUSED_PAD src0_sel:WORD_1
	v_cvt_f32_f16_e32 v70, v54
	v_cmp_lt_f32_e32 vcc, 0, v61
	v_cvt_f32_f16_e32 v54, v55
	v_pk_add_f32 v[62:63], v[62:63], v[64:65]
	v_cndmask_b32_e32 v42, v59, v61, vcc
	v_pk_fma_f32 v[62:63], v[102:103], v[70:71], v[62:63] op_sel_hi:[0,1,1]
	v_pk_mul_f32 v[108:109], v[18:19], v[62:63] op_sel_hi:[0,1]
	v_mul_f32_e32 v50, 0x3fb8aa3b, v108
	v_exp_f32_e32 v62, v50
	v_mul_f32_e32 v50, 0x3fb8aa3b, v109
	v_exp_f32_e32 v63, v50
	v_cmp_lt_f32_e32 vcc, 0, v60
	v_cvt_f32_f16_sdwa v55, v55 dst_sel:DWORD dst_unused:UNUSED_PAD src0_sel:WORD_1
	s_movk_i32 s1, 0x44
	v_cndmask_b32_e32 v50, v58, v60, vcc
	v_pk_add_f32 v[110:111], v[62:63], -1.0 op_sel_hi:[1,0]
	global_load_dwordx4 v[58:61], v106, s[4:5] offset:176
	global_load_dwordx4 v[62:65], v106, s[4:5] offset:160
	global_load_dwordx4 v[70:73], v106, s[4:5] offset:144
	global_load_dwordx4 v[74:77], v106, s[4:5] offset:128
	global_load_dwordx4 v[78:81], v106, s[4:5] offset:112
	global_load_dwordx4 v[82:85], v106, s[4:5] offset:96
	global_load_dwordx4 v[86:89], v106, s[4:5] offset:80
	global_load_dwordx4 v[90:93], v106, s[4:5] offset:64
	v_cvt_pk_f16_f32 v97, v50, v42
	v_cvt_f32_f16_e32 v42, v43
	v_cvt_f32_f16_sdwa v43, v43 dst_sel:DWORD dst_unused:UNUSED_PAD src0_sel:WORD_1
	v_cvt_f32_f16_e32 v50, v51
	v_cvt_f32_f16_sdwa v51, v51 dst_sel:DWORD dst_unused:UNUSED_PAD src0_sel:WORD_1
	v_cmp_lt_f32_e32 vcc, 0, v109
	v_cvt_f32_f16_e32 v106, v52
	v_cvt_f32_f16_e32 v52, v53
	v_cndmask_b32_e32 v103, v111, v109, vcc
	v_pk_add_f32 v[42:43], v[42:43], v[50:51]
	v_cmp_lt_f32_e32 vcc, 0, v108
	v_pk_fma_f32 v[42:43], v[102:103], v[54:55], v[42:43] op_sel_hi:[0,1,1]
	v_cvt_f32_f16_e32 v54, v44
	v_cvt_f32_f16_sdwa v55, v44 dst_sel:DWORD dst_unused:UNUSED_PAD src0_sel:WORD_1
	v_cndmask_b32_e32 v110, v110, v108, vcc
	v_pk_mul_f32 v[42:43], v[18:19], v[42:43] op_sel_hi:[0,1]
	v_cvt_f32_f16_e32 v108, v56
	v_cvt_f32_f16_sdwa v109, v56 dst_sel:DWORD dst_unused:UNUSED_PAD src0_sel:WORD_1
	v_mul_f32_e32 v50, 0x3fb8aa3b, v42
	v_mul_f32_e32 v51, 0x3fb8aa3b, v43
	v_exp_f32_e32 v50, v50
	v_exp_f32_e32 v51, v51
	v_pk_add_f32 v[54:55], v[54:55], v[106:107]
	v_cmp_lt_f32_e32 vcc, 0, v43
	v_pk_fma_f32 v[54:55], v[102:103], v[108:109], v[54:55] op_sel_hi:[0,1,1]
	v_pk_mul_f32 v[54:55], v[18:19], v[54:55] op_sel_hi:[0,1]
	v_pk_add_f32 v[50:51], v[50:51], -1.0 op_sel_hi:[1,0]
	v_mul_f32_e32 v44, 0x3fb8aa3b, v54
	v_cndmask_b32_e32 v43, v51, v43, vcc
	v_exp_f32_e32 v106, v44
	v_mul_f32_e32 v44, 0x3fb8aa3b, v55
	v_cmp_lt_f32_e32 vcc, 0, v42
	v_exp_f32_e32 v107, v44
	v_cvt_f32_f16_sdwa v53, v53 dst_sel:DWORD dst_unused:UNUSED_PAD src0_sel:WORD_1
	v_cndmask_b32_e32 v44, v50, v42, vcc
	v_cvt_pk_f16_f32 v43, v44, v43
	v_cvt_f32_f16_e32 v44, v45
	v_cvt_f32_f16_sdwa v45, v45 dst_sel:DWORD dst_unused:UNUSED_PAD src0_sel:WORD_1
	v_cvt_f32_f16_e32 v56, v57
	v_cvt_f32_f16_sdwa v57, v57 dst_sel:DWORD dst_unused:UNUSED_PAD src0_sel:WORD_1
	v_pk_add_f32 v[50:51], v[106:107], -1.0 op_sel_hi:[1,0]
	v_pk_add_f32 v[44:45], v[44:45], v[52:53]
	v_cmp_lt_f32_e32 vcc, 0, v55
	v_pk_fma_f32 v[44:45], v[102:103], v[56:57], v[44:45] op_sel_hi:[0,1,1]
	v_pk_mul_f32 v[52:53], v[18:19], v[44:45] op_sel_hi:[0,1]
	v_mul_f32_e32 v18, 0x3fb8aa3b, v52
	v_exp_f32_e32 v56, v18
	v_mul_f32_e32 v18, 0x3fb8aa3b, v53
	v_exp_f32_e32 v57, v18
	v_cndmask_b32_e32 v51, v51, v55, vcc
	v_cmp_lt_f32_e32 vcc, 0, v54
	v_cvt_pk_f16_f32 v42, v110, v103
	s_nop 0
	v_cndmask_b32_e32 v18, v50, v54, vcc
	v_cvt_pk_f16_f32 v44, v18, v51
	v_pk_add_f32 v[50:51], v[56:57], -1.0 op_sel_hi:[1,0]
	v_cmp_lt_f32_e32 vcc, 0, v53
	s_nop 1
	v_cndmask_b32_e32 v18, v51, v53, vcc
	v_cmp_lt_f32_e32 vcc, 0, v52
	s_nop 1
	v_cndmask_b32_e32 v45, v50, v52, vcc
	v_cvt_pk_f16_f32 v45, v45, v18
	v_lshrrev_b32_e32 v18, 4, v0
	v_mov_b32_e32 v50, 0x3300
	v_mad_u32_u24 v54, v18, s0, v50
	v_mov_b32_e32 v50, 0x3308
	v_mad_u32_u24 v57, v18, s0, v50
	v_mov_b32_e32 v50, 0x3310
	v_mad_u32_u24 v102, v18, s0, v50
	v_mov_b32_e32 v50, 0x3318
	v_mad_u32_u24 v103, v18, s0, v50
	v_mov_b32_e32 v50, 0x3320
	v_mad_u32_u24 v106, v18, s0, v50
	v_mov_b32_e32 v50, 0x3340
	v_mad_u32_u24 v107, v18, s0, v50
	v_mov_b32_e32 v50, 0x3360
	v_mad_u32_u24 v108, v18, s0, v50
	v_mov_b32_e32 v50, 0x3380
	v_mad_u32_u24 v109, v18, s0, v50
	v_mov_b32_e32 v50, 0x33a0
	v_add_u32_e32 v55, v54, v98
	v_mad_u32_u24 v56, v18, s1, v98
	v_mad_u32_u24 v110, v18, s0, v50
	v_cvt_pk_f16_f32 v19, v19, v20
	v_cvt_pk_f16_f32 v20, v21, v30
	v_cvt_pk_f16_f32 v21, v31, v32
	v_pack_b32_f16 v50, v104, v19
	v_alignbit_b32 v51, v20, v19, 16
	v_alignbit_b32 v52, v21, v20, 16
	v_alignbit_b32 v53, v105, v21, 16
	v_cvt_pk_f16_f32 v19, v27, v28
	v_cvt_pk_f16_f32 v22, v29, v22
	v_mfma_f32_16x16x32_f16 a[0:3], v[34:37], v[50:53], 0
	v_cvt_pk_f16_f32 v23, v23, v24
	v_pack_b32_f16 v20, v26, v19
	v_alignbit_b32 v21, v22, v19, 16
	v_mfma_f32_16x16x32_f16 a[4:7], v[46:49], v[50:53], 0
	v_alignbit_b32 v22, v23, v22, 16
	v_alignbit_b32 v23, v25, v23, 16
	s_cmpk_eq_i32 s2, 0xbf
	v_mfma_f32_16x16x32_f16 a[8:11], v[94:97], v[50:53], 0
	v_mfma_f32_16x16x32_f16 a[0:3], v[38:41], v[20:23], a[0:3]
	s_nop 7
	ds_write_b32 v33, a0
	ds_write_b32 v33, a1 offset:68
	ds_write_b32 v33, a2 offset:136
	v_mfma_f32_16x16x32_f16 a[4:7], v[66:69], v[20:23], a[4:7]
	v_mfma_f32_16x16x32_f16 a[8:11], v[42:45], v[20:23], a[8:11]
	ds_write_b32 v33, a3 offset:204
	s_nop 5
	ds_write_b32 v33, a4 offset:4352
	ds_write_b32 v33, a5 offset:4420
	ds_write_b32 v33, a6 offset:4488
	ds_write_b32 v33, a7 offset:4556
	ds_write_b32 v33, a8 offset:8704
	ds_write_b32 v33, a9 offset:8772
	ds_write_b32 v33, a10 offset:8840
	ds_write_b32 v33, a11 offset:8908
	s_waitcnt lgkmcnt(0)
	s_barrier
	ds_read_b32 v20, v56 offset:8704
	ds_read_b32 v22, v56 offset:9792
	ds_read_b32 v24, v56 offset:10880
	ds_read_b32 v26, v56 offset:11968
	ds_read_b32 v21, v56 offset:4352
	ds_read_b32 v23, v56 offset:5440
	ds_read_b32 v25, v56 offset:6528
	ds_read_b32 v27, v56 offset:7616
	ds_read_b32 v19, v56
	ds_read_b32 v28, v56 offset:1088
	ds_read_b32 v29, v56 offset:2176
	ds_read_b32 v30, v56 offset:3264
	s_waitcnt lgkmcnt(6)
	v_pk_add_f32 v[20:21], v[20:21], v[22:23]
	s_waitcnt lgkmcnt(2)
	v_add_f32_e32 v19, v19, v28
	s_waitcnt lgkmcnt(1)
	v_add_f32_e32 v19, v19, v29
	v_pk_add_f32 v[20:21], v[20:21], v[24:25]
	s_waitcnt lgkmcnt(0)
	v_add_f32_e32 v19, v19, v30
	v_pk_add_f32 v[20:21], v[20:21], v[26:27]
	v_add_f32_e32 v19, v100, v19
	v_mul_f32_e32 v22, 0x3fb8aa3b, v19
	v_pk_add_f32 v[20:21], v[100:101], v[20:21] op_sel_hi:[0,1]
	v_exp_f32_e32 v22, v22
	v_mul_f32_e32 v23, 0x3fb8aa3b, v21
	v_exp_f32_e32 v23, v23
	v_cmp_lt_f32_e32 vcc, 0, v19
	v_add_f32_e32 v22, -1.0, v22
	s_nop 0
	v_cndmask_b32_e32 v19, v22, v19, vcc
	v_add_f32_e32 v22, -1.0, v23
	v_mul_f32_e32 v23, 0x3fb8aa3b, v20
	v_exp_f32_e32 v23, v23
	v_cmp_lt_f32_e32 vcc, 0, v21
	s_nop 1
	v_cndmask_b32_e32 v21, v22, v21, vcc
	ds_write2_b32 v55, v19, v21 offset1:16
	v_add_f32_e32 v19, -1.0, v23
	v_cmp_lt_f32_e32 vcc, 0, v20
	s_nop 1
	v_cndmask_b32_e32 v19, v19, v20, vcc
	ds_write_b32 v55, v19 offset:128
	s_waitcnt lgkmcnt(0)
	s_barrier
	ds_read2_b32 v[20:21], v54 offset1:1
	ds_read2_b32 v[22:23], v57 offset1:1
	ds_read2_b32 v[24:25], v102 offset1:1
	ds_read2_b32 v[26:27], v103 offset1:1
	s_waitcnt lgkmcnt(3)
	v_mul_f32_e32 v19, v21, v15
	v_fmac_f32_e32 v19, v20, v14
	s_waitcnt lgkmcnt(2)
	v_fmac_f32_e32 v19, v22, v16
	s_waitcnt lgkmcnt(1)
	v_mul_f32_e32 v16, v25, v11
	v_fmac_f32_e32 v16, v24, v10
	v_mov_b32_e32 v11, 0x3338
	v_fmac_f32_e32 v19, v23, v17
	s_waitcnt lgkmcnt(0)
	v_fmac_f32_e32 v16, v26, v12
	v_mov_b32_e32 v10, 0x3330
	v_mad_u32_u24 v14, v18, s0, v11
	v_mov_b32_e32 v11, 0x3328
	v_fmac_f32_e32 v16, v27, v13
	v_mad_u32_u24 v10, v18, s0, v10
	v_mad_u32_u24 v12, v18, s0, v11
	v_add_f32_e32 v17, v101, v19
	ds_read2_b32 v[10:11], v10 offset1:1
	ds_read2_b32 v[12:13], v12 offset1:1
	ds_read2_b32 v[14:15], v14 offset1:1
	v_add_f32_e32 v19, v17, v16
	ds_read2_b32 v[16:17], v106 offset1:1
	s_waitcnt lgkmcnt(3)
	v_pk_mul_f32 v[2:3], v[10:11], v[2:3]
	s_waitcnt lgkmcnt(2)
	v_pk_mul_f32 v[8:9], v[12:13], v[8:9]
	s_waitcnt lgkmcnt(1)
	v_pk_mul_f32 v[4:5], v[14:15], v[4:5]
	v_mov_b32_e32 v11, v2
	s_waitcnt lgkmcnt(0)
	v_pk_mul_f32 v[6:7], v[16:17], v[6:7]
	ds_read2_b32 v[12:13], v107 offset1:1
	ds_read2_b32 v[14:15], v108 offset1:1
	ds_read2_b32 v[20:21], v109 offset1:1
	v_mov_b32_e32 v10, v6
	v_mov_b32_e32 v2, v7
	v_pk_add_f32 v[2:3], v[10:11], v[2:3]
	v_mov_b32_e32 v6, v8
	v_mov_b32_e32 v7, v4
	v_pk_add_f32 v[2:3], v[2:3], v[6:7]
	v_mov_b32_e32 v4, v9
	v_pk_add_f32 v[2:3], v[2:3], v[4:5]
	v_mov_b32_e32 v4, 0x3350
	v_mad_u32_u24 v10, v18, s0, v4
	v_mov_b32_e32 v4, 0x3358
	v_mad_u32_u24 v6, v18, s0, v4
	v_mov_b32_e32 v4, 0x3348
	v_mov_b32_e32 v5, 0x3370
	v_mad_u32_u24 v4, v18, s0, v4
	v_mad_u32_u24 v8, v18, s0, v5
	ds_read2_b32 v[16:17], v110 offset1:1
	ds_read2_b32 v[4:5], v4 offset1:1
	ds_read2_b32 v[6:7], v6 offset1:1
	ds_read2_b32 v[8:9], v8 offset1:1
	ds_read2_b32 v[10:11], v10 offset1:1
	v_add_f32_e32 v2, v19, v2
	v_add_f32_e32 v19, v2, v3
	s_waitcnt vmcnt(0) lgkmcnt(3)
	v_pk_mul_f32 v[2:3], v[4:5], v[92:93]
	s_waitcnt lgkmcnt(2)
	v_pk_mul_f32 v[4:5], v[6:7], v[88:89]
	v_pk_mul_f32 v[6:7], v[12:13], v[90:91]
	s_waitcnt lgkmcnt(0)
	v_pk_mul_f32 v[10:11], v[10:11], v[86:87]
	v_mov_b32_e32 v12, v6
	v_mov_b32_e32 v13, v10
	v_mov_b32_e32 v10, v7
	v_pk_add_f32 v[6:7], v[12:13], v[10:11]
	v_mov_b32_e32 v10, v2
	v_mov_b32_e32 v11, v4
	v_pk_add_f32 v[6:7], v[6:7], v[10:11]
	v_mov_b32_e32 v4, v3
	v_pk_add_f32 v[2:3], v[6:7], v[4:5]
	v_pk_mul_f32 v[12:13], v[14:15], v[82:83]
	v_add_f32_e32 v2, v19, v2
	v_add_f32_e32 v19, v2, v3
	v_mov_b32_e32 v2, 0x3378
	v_mov_b32_e32 v3, 0x3368
	v_mad_u32_u24 v2, v18, s0, v2
	v_mad_u32_u24 v4, v18, s0, v3
	ds_read2_b32 v[2:3], v2 offset1:1
	ds_read2_b32 v[4:5], v4 offset1:1
	v_pk_mul_f32 v[8:9], v[8:9], v[78:79]
	v_mov_b32_e32 v14, v12
	v_mov_b32_e32 v15, v8
	s_waitcnt lgkmcnt(1)
	v_pk_mul_f32 v[2:3], v[2:3], v[80:81]
	s_waitcnt lgkmcnt(0)
	v_pk_mul_f32 v[4:5], v[4:5], v[84:85]
	v_mov_b32_e32 v8, v13
	v_pk_add_f32 v[8:9], v[14:15], v[8:9]
	v_mov_b32_e32 v12, v4
	v_mov_b32_e32 v13, v2
	v_pk_add_f32 v[8:9], v[8:9], v[12:13]
	v_mov_b32_e32 v2, v5
	v_pk_add_f32 v[2:3], v[8:9], v[2:3]
	v_mov_b32_e32 v6, 0x3390
	v_add_f32_e32 v2, v19, v2
	v_mov_b32_e32 v7, 0x3398
	v_add_f32_e32 v19, v2, v3
	v_mov_b32_e32 v2, 0x3388
	v_mad_u32_u24 v6, v18, s0, v6
	v_mad_u32_u24 v10, v18, s0, v7
	v_mad_u32_u24 v2, v18, s0, v2
	ds_read2_b32 v[6:7], v6 offset1:1
	ds_read2_b32 v[10:11], v10 offset1:1
	ds_read2_b32 v[2:3], v2 offset1:1
	v_mov_b32_e32 v5, 0x33b8
	v_mov_b32_e32 v4, 0x33b0
	v_mad_u32_u24 v8, v18, s0, v5
	v_mov_b32_e32 v5, 0x33a8
	v_mad_u32_u24 v4, v18, s0, v4
	v_mad_u32_u24 v12, v18, s0, v5
	v_pk_mul_f32 v[14:15], v[20:21], v[74:75]
	s_waitcnt lgkmcnt(2)
	v_pk_mul_f32 v[6:7], v[6:7], v[70:71]
	ds_read2_b32 v[4:5], v4 offset1:1
	ds_read2_b32 v[8:9], v8 offset1:1
	ds_read2_b32 v[12:13], v12 offset1:1
	s_waitcnt lgkmcnt(3)
	v_pk_mul_f32 v[2:3], v[2:3], v[76:77]
	v_pk_mul_f32 v[10:11], v[10:11], v[72:73]
	v_mov_b32_e32 v20, v14
	v_mov_b32_e32 v21, v6
	v_mov_b32_e32 v6, v15
	v_pk_add_f32 v[6:7], v[20:21], v[6:7]
	v_mov_b32_e32 v14, v2
	v_mov_b32_e32 v15, v10
	v_pk_add_f32 v[6:7], v[6:7], v[14:15]
	v_mov_b32_e32 v10, v3
	v_pk_add_f32 v[2:3], v[6:7], v[10:11]
	s_waitcnt lgkmcnt(1)
	v_pk_mul_f32 v[6:7], v[8:9], v[60:61]
	v_add_f32_e32 v2, v19, v2
	v_pk_mul_f32 v[8:9], v[16:17], v[62:63]
	v_pk_mul_f32 v[4:5], v[4:5], v[58:59]
	v_add_f32_e32 v14, v2, v3
	s_waitcnt lgkmcnt(0)
	v_pk_mul_f32 v[2:3], v[12:13], v[64:65]
	v_mov_b32_e32 v10, v8
	v_mov_b32_e32 v11, v4
	v_mov_b32_e32 v4, v9
	v_pk_add_f32 v[4:5], v[10:11], v[4:5]
	v_mov_b32_e32 v8, v2
	v_mov_b32_e32 v9, v6
	v_pk_add_f32 v[4:5], v[4:5], v[8:9]
	v_mov_b32_e32 v6, v3
	v_pk_add_f32 v[2:3], v[4:5], v[6:7]
	s_mov_b32 s0, 0x800000
	v_add_f32_e32 v2, v14, v2
	v_add_f32_e32 v8, v2, v3
	s_nop 1
	v_mov_b32_dpp v5, v8 row_ror:8 row_mask:0xf bank_mask:0xf
	v_max_f32_e32 v5, v5, v5
	v_max_f32_e32 v6, v8, v5
	s_nop 1
	v_mov_b32_dpp v7, v6 row_ror:4 row_mask:0xf bank_mask:0xf
	v_max_f32_e32 v7, v7, v7
	v_max_f32_e32 v7, v6, v7
	s_nop 1
	v_mov_b32_dpp v9, v7 row_ror:2 row_mask:0xf bank_mask:0xf
	v_max_f32_e32 v9, v9, v9
	v_max_f32_e32 v9, v7, v9
	s_nop 1
	v_mov_b32_dpp v10, v9 row_ror:1 row_mask:0xf bank_mask:0xf
	v_max_f32_e32 v10, v10, v10
	v_max_f32_e32 v9, v9, v10
	v_sub_f32_e32 v8, v8, v9
	v_mul_f32_e32 v9, 0x3fb8aa3b, v8
	v_exp_f32_e32 v9, v9
	s_nop 1
	v_mov_b32_dpp v10, v9 row_ror:8 row_mask:0xf bank_mask:0xf
	v_add_f32_e32 v9, v9, v10
	s_nop 1
	v_mov_b32_dpp v10, v9 row_ror:4 row_mask:0xf bank_mask:0xf
	v_add_f32_e32 v9, v9, v10
	s_nop 1
	v_mov_b32_dpp v10, v9 row_ror:2 row_mask:0xf bank_mask:0xf
	v_add_f32_e32 v9, v9, v10
	s_nop 1
	v_mov_b32_dpp v10, v9 row_ror:1 row_mask:0xf bank_mask:0xf
	v_add_f32_e32 v9, v9, v10
	v_cmp_gt_f32_e32 vcc, s0, v9
	s_mov_b32 s0, 0x3f317217
	s_nop 0
	v_cndmask_b32_e64 v10, 0, 32, vcc
	v_ldexp_f32 v9, v9, v10
	v_log_f32_e32 v9, v9
	s_nop 0
	v_mul_f32_e32 v10, 0x3f317217, v9
	v_fma_f32 v10, v9, s0, -v10
	v_fmamk_f32 v10, v9, 0x3377d1cf, v10
	s_mov_b32 s0, 0x7f800000
	v_fmac_f32_e32 v10, 0x3f317217, v9
	v_cmp_lt_f32_e64 s[0:1], |v9|, s0
	s_nop 1
	v_cndmask_b32_e64 v9, v9, v10, s[0:1]
	v_mov_b32_e32 v10, 0x41b17218
	v_cndmask_b32_e32 v10, 0, v10, vcc
	v_sub_f32_e32 v9, v9, v10
	v_sub_f32_e32 v10, v8, v9
	v_or_b32_e32 v8, s3, v18
	v_ashrrev_i32_e32 v9, 31, v8
	v_lshlrev_b64 v[8:9], 6, v[8:9]
	v_lshl_add_u64 v[8:9], s[8:9], 0, v[8:9]
	s_cselect_b64 s[0:1], -1, 0
	v_cmp_eq_u32_e32 vcc, 3, v1
	v_lshl_add_u64 v[8:9], v[8:9], 0, v[98:99]
	s_and_b64 s[0:1], s[0:1], vcc
	global_store_dword v[8:9], v10, off
